# attention tile loops: one static s_setprio 1 for waves 4-7 before the loop (reset after it), on top of the widened epilogue stores
# baseline (speedup 1.0000x reference)
; #define LAS __attribute__((address_space(3)))
; __device__ __forceinline__ float bf2f(short s) { return __uint_as_float(((unsigned)(unsigned short)s) << 16); }
; __device__ __forceinline__ void attn_unit(LAS unsigned char* lds, const bf16_t* Q, const bf16_t* K, const bf16_t* Vt, const float* kmean, bf16_t* mix,
;                                           const int b, const int h, const int blk, const int wv) {
;     ...
;     {
;         float g[7];
; #pragma unroll
;         for (int n = 0; n < 7; ++n) {
;             float p = 0.f;
;             if (n < blk) {
; #pragma unroll
;                 for (int ks = 0; ks < 8; ++ks) {
;                     const f32x4 k0 = *(const LAS f32x4*)&km[n * 128 + 16 * ks + 8 * hh], k1 = *(const LAS f32x4*)&km[n * 128 + 16 * ks + 8 * hh + 4];
;                     p += bf2f(qf[ks][0]) * k0[0] + bf2f(qf[ks][1]) * k0[1] + bf2f(qf[ks][2]) * k0[2] + bf2f(qf[ks][3]) * k0[3]
;                        + bf2f(qf[ks][4]) * k1[0] + bf2f(qf[ks][5]) * k1[1] + bf2f(qf[ks][6]) * k1[2] + bf2f(qf[ks][7]) * k1[3];
;                 }
;             }
;             g[n] = p + __shfl_xor(p, 32);
;         }
; #pragma unroll
;         for (int n = 0; n < 7; ++n) {
;             int rank = 0;
; #pragma unroll
;             for (int m2 = 0; m2 < 7; ++m2) if (m2 != n && m2 < blk) rank += (g[m2] > g[n] || (g[m2] == g[n] && m2 < n)) ? 1 : 0;
;             if (n < blk && rank < 3) sel |= 1u << n;
;         }
.LBB0_702:
	s_andn2_b64 vcc, exec, s[36:37]
	s_mov_b32 s33, 0
	s_cbranch_vccnz .LBB0_764
	v_add_f32_e32 v6, v70, v73
	v_add_f32_e32 v7, v71, v72
	v_add_f32_e32 v5, v75, v76
	v_cmp_gt_f32_e32 vcc, v6, v7
	v_add_f32_e32 v4, v74, v77
	s_and_b64 s[34:35], s[2:3], vcc
	v_cmp_gt_f32_e32 vcc, v5, v7
	v_add_f32_e32 v3, v79, v81
	v_cndmask_b32_e64 v8, 0, 1, s[34:35]
	s_and_b64 s[34:35], s[4:5], vcc
	v_cmp_gt_f32_e32 vcc, v4, v7
	v_add_f32_e32 v2, v78, v82
	v_cndmask_b32_e64 v9, 0, 1, s[34:35]
	s_and_b64 s[34:35], s[6:7], vcc
	v_cmp_gt_f32_e32 vcc, v3, v7
	v_add_f32_e32 v1, v83, v1
	v_add_u32_e32 v8, v9, v8
	v_cndmask_b32_e64 v9, 0, 1, s[34:35]
	s_and_b64 s[34:35], s[8:9], vcc
	v_cmp_gt_f32_e32 vcc, v2, v7
	v_cndmask_b32_e64 v10, 0, 1, s[34:35]
	s_and_b64 s[34:35], s[28:29], vcc
	v_cmp_gt_f32_e32 vcc, v1, v7
	v_add3_u32 v8, v8, v9, v10
	v_cndmask_b32_e64 v9, 0, 1, s[34:35]
	s_and_b64 s[34:35], s[30:31], vcc
	v_cndmask_b32_e64 v10, 0, 1, s[34:35]
	v_add3_u32 v8, v8, v9, v10
	v_cmp_gt_u32_e32 vcc, 3, v8
	s_and_b64 s[34:35], s[0:1], vcc
	v_cmp_ge_f32_e32 vcc, v7, v6
	v_cndmask_b32_e64 v8, 0, 1, s[34:35]
	s_and_b64 s[34:35], s[0:1], vcc
	v_cmp_gt_f32_e32 vcc, v5, v6
	v_cndmask_b32_e64 v9, 0, 1, s[34:35]
	s_and_b64 s[34:35], s[4:5], vcc
	v_cmp_gt_f32_e32 vcc, v4, v6
	v_cndmask_b32_e64 v10, 0, 1, s[34:35]
	s_and_b64 s[34:35], s[6:7], vcc
	v_cmp_gt_f32_e32 vcc, v3, v6
	v_add_u32_e32 v9, v10, v9
	v_cndmask_b32_e64 v10, 0, 1, s[34:35]
	s_and_b64 s[34:35], s[8:9], vcc
	v_cmp_gt_f32_e32 vcc, v2, v6
	v_cndmask_b32_e64 v11, 0, 1, s[34:35]
	s_and_b64 s[34:35], s[28:29], vcc
	v_cmp_gt_f32_e32 vcc, v1, v6
	v_add3_u32 v9, v9, v10, v11
	v_cndmask_b32_e64 v10, 0, 1, s[34:35]
	s_and_b64 s[34:35], s[30:31], vcc
	v_cndmask_b32_e64 v11, 0, 1, s[34:35]
	v_add3_u32 v9, v9, v10, v11
	v_cmp_gt_u32_e32 vcc, 3, v9
	s_and_b64 s[34:35], s[2:3], vcc
	v_cmp_ge_f32_e32 vcc, v7, v5
	v_cndmask_b32_e64 v9, 0, 2, s[34:35]
	s_and_b64 s[34:35], s[0:1], vcc
	v_cmp_ge_f32_e32 vcc, v6, v5
	v_cndmask_b32_e64 v10, 0, 1, s[34:35]
	s_and_b64 s[34:35], s[2:3], vcc
	v_cmp_gt_f32_e32 vcc, v4, v5
	v_cndmask_b32_e64 v11, 0, 1, s[34:35]
	s_and_b64 s[34:35], s[6:7], vcc
	v_cmp_gt_f32_e32 vcc, v3, v5
	v_add_u32_e32 v10, v10, v11
	v_cndmask_b32_e64 v11, 0, 1, s[34:35]
	s_and_b64 s[34:35], s[8:9], vcc
	v_cmp_gt_f32_e32 vcc, v2, v5
	v_cndmask_b32_e64 v12, 0, 1, s[34:35]
	s_and_b64 s[34:35], s[28:29], vcc
	v_cmp_gt_f32_e32 vcc, v1, v5
	v_add3_u32 v10, v10, v11, v12
	v_cndmask_b32_e64 v11, 0, 1, s[34:35]
	s_and_b64 s[34:35], s[30:31], vcc
	v_cndmask_b32_e64 v12, 0, 1, s[34:35]
	v_add3_u32 v10, v10, v11, v12
	v_cmp_gt_u32_e32 vcc, 3, v10
	s_and_b64 s[34:35], s[4:5], vcc
	v_cmp_ge_f32_e32 vcc, v7, v4
	v_cndmask_b32_e64 v10, 0, 4, s[34:35]
	s_and_b64 s[34:35], s[0:1], vcc
	v_cmp_ge_f32_e32 vcc, v6, v4
	v_or3_b32 v8, v9, v8, v10
	v_cndmask_b32_e64 v9, 0, 1, s[34:35]
	s_and_b64 s[34:35], s[2:3], vcc
	v_cmp_ge_f32_e32 vcc, v5, v4
	v_cndmask_b32_e64 v10, 0, 1, s[34:35]
	s_and_b64 s[34:35], s[4:5], vcc
	v_cmp_gt_f32_e32 vcc, v3, v4
	v_add_u32_e32 v9, v9, v10
	v_cndmask_b32_e64 v10, 0, 1, s[34:35]
	s_and_b64 s[34:35], s[8:9], vcc
	v_cmp_gt_f32_e32 vcc, v2, v4
	v_cndmask_b32_e64 v11, 0, 1, s[34:35]
	s_and_b64 s[34:35], s[28:29], vcc
	v_cmp_gt_f32_e32 vcc, v1, v4
	v_add3_u32 v9, v9, v10, v11
	v_cndmask_b32_e64 v10, 0, 1, s[34:35]
	s_and_b64 s[34:35], s[30:31], vcc
	v_cndmask_b32_e64 v11, 0, 1, s[34:35]
	v_add3_u32 v9, v9, v10, v11
	v_cmp_gt_u32_e32 vcc, 3, v9
	s_and_b64 s[34:35], s[6:7], vcc
	v_cmp_ge_f32_e32 vcc, v7, v3
	v_cndmask_b32_e64 v9, 0, 8, s[34:35]
	s_and_b64 s[34:35], s[0:1], vcc
	v_cmp_ge_f32_e32 vcc, v6, v3
	v_cndmask_b32_e64 v10, 0, 1, s[34:35]
	s_and_b64 s[34:35], s[2:3], vcc
	v_cmp_ge_f32_e32 vcc, v5, v3
	v_cndmask_b32_e64 v11, 0, 1, s[34:35]
	s_and_b64 s[34:35], s[4:5], vcc
	v_cmp_ge_f32_e32 vcc, v4, v3
	v_add_u32_e32 v10, v10, v11
	v_cndmask_b32_e64 v11, 0, 1, s[34:35]
	s_and_b64 s[34:35], s[6:7], vcc
	v_cmp_gt_f32_e32 vcc, v2, v3
	v_cndmask_b32_e64 v12, 0, 1, s[34:35]
	s_and_b64 s[34:35], s[28:29], vcc
	v_cmp_gt_f32_e32 vcc, v1, v3
	v_add3_u32 v10, v10, v11, v12
	v_cndmask_b32_e64 v11, 0, 1, s[34:35]
	s_and_b64 s[34:35], s[30:31], vcc
	v_cndmask_b32_e64 v12, 0, 1, s[34:35]
	v_add3_u32 v10, v10, v11, v12
	v_cmp_gt_u32_e32 vcc, 3, v10
	s_and_b64 s[34:35], s[8:9], vcc
	v_cmp_ge_f32_e32 vcc, v7, v2
	v_cndmask_b32_e64 v10, 0, 16, s[34:35]
	s_and_b64 s[34:35], s[0:1], vcc
	v_cmp_ge_f32_e32 vcc, v6, v2
	v_or3_b32 v8, v8, v9, v10
	v_cndmask_b32_e64 v9, 0, 1, s[34:35]
; #define ATT_LOAD(kr, vr, ti) do { const int _k0 = ATT_KEY0(ti); _Pragma("unroll") for (int _i = 0; _i < 2; ++_i) { const int _c = tid + 512 * _i; \
;         kr[_i] = *(const u32x4*)(K + (hbase + _k0) * 128 + (size_t)_c * 8); \
;         vr[_i] = *(const u32x4*)(Vt + (hbase + _k0) * 128 + (size_t)_c * 8); } } while (0)
; #define ATT_STORE(kr, vr, buf) do { _Pragma("unroll") for (int _i = 0; _i < 2; ++_i) { const int _c = tid + 512 * _i; \
;         *(LAS u32x4*)(lds + L_K + (buf) * KT_BYTES + (_c >> 4) * KSTR + (_c & 15) * 16) = kr[_i]; \
;         *(LAS u32x4*)(lds + L_V + (buf) * VT_BYTES + (_c >> 4) * VSTR + (_c & 15) * 16) = vr[_i]; } } while (0)
; __device__ __forceinline__ void attn_unit(LAS unsigned char* lds, const bf16_t* Q, const bf16_t* K, const bf16_t* Vt, const float* kmean, bf16_t* mix,
;                                           const int b, const int h, const int blk, const int wv) {
;     ...
;         for (int n = 0; n < 7; ++n) {
;             int rank = 0;
; #pragma unroll
;             for (int m2 = 0; m2 < 7; ++m2) if (m2 != n && m2 < blk) rank += (g[m2] > g[n] || (g[m2] == g[n] && m2 < n)) ? 1 : 0;
;             if (n < blk && rank < 3) sel |= 1u << n;
;         }
;     }
;     ATT_STORE(krA, vrA, 0);
;     if (ntile > 1) ATT_LOAD(krA, vrA, 1);
;     __syncthreads();
;     f32x16 o[4];
; #pragma unroll
;     for (int d = 0; d < 4; ++d)
; #pragma unroll
;         for (int r = 0; r < 16; ++r) o[d][r] = 0.f;
;     float mrun = -1e30f, lsum = 0.f;
	s_and_b64 s[34:35], s[2:3], vcc
	v_cmp_ge_f32_e32 vcc, v5, v2
	v_cndmask_b32_e64 v10, 0, 1, s[34:35]
	s_and_b64 s[34:35], s[4:5], vcc
	v_cmp_ge_f32_e32 vcc, v4, v2
	v_add_u32_e32 v9, v9, v10
	v_cndmask_b32_e64 v10, 0, 1, s[34:35]
	s_and_b64 s[34:35], s[6:7], vcc
	v_cmp_ge_f32_e32 vcc, v3, v2
	v_cndmask_b32_e64 v11, 0, 1, s[34:35]
	s_and_b64 s[34:35], s[8:9], vcc
	v_cmp_gt_f32_e32 vcc, v1, v2
	v_add3_u32 v9, v9, v10, v11
	v_cndmask_b32_e64 v10, 0, 1, s[34:35]
	s_and_b64 s[34:35], s[30:31], vcc
	v_cndmask_b32_e64 v11, 0, 1, s[34:35]
	v_add3_u32 v9, v9, v10, v11
	v_cmp_gt_u32_e32 vcc, 3, v9
	s_and_b64 s[34:35], s[28:29], vcc
	v_cmp_ge_f32_e32 vcc, v7, v1
	s_and_b64 s[0:1], s[0:1], vcc
	v_cmp_ge_f32_e32 vcc, v6, v1
	v_cndmask_b32_e64 v7, 0, 1, s[0:1]
	s_and_b64 s[0:1], s[2:3], vcc
	v_cmp_ge_f32_e32 vcc, v5, v1
	v_cndmask_b32_e64 v6, 0, 1, s[0:1]
	s_and_b64 s[0:1], s[4:5], vcc
	v_cmp_ge_f32_e32 vcc, v4, v1
	v_cndmask_b32_e64 v5, 0, 1, s[0:1]
	s_and_b64 s[0:1], s[6:7], vcc
	v_cmp_ge_f32_e32 vcc, v3, v1
	v_cndmask_b32_e64 v4, 0, 1, s[0:1]
	s_and_b64 s[0:1], s[8:9], vcc
	v_cmp_ge_f32_e32 vcc, v2, v1
	v_add_u32_e32 v6, v7, v6
	v_cndmask_b32_e64 v3, 0, 1, s[0:1]
	s_and_b64 s[0:1], s[28:29], vcc
	v_add3_u32 v4, v6, v5, v4
	v_cndmask_b32_e64 v1, 0, 1, s[0:1]
	v_add3_u32 v1, v4, v3, v1
	v_cmp_gt_u32_e32 vcc, 3, v1
	s_and_b64 s[0:1], s[30:31], vcc
	v_cndmask_b32_e64 v9, 0, 32, s[34:35]
	v_cndmask_b32_e64 v1, 0, 64, s[0:1]
	v_or3_b32 v176, v8, v9, v1
	v_lshrrev_b32_e32 v1, 2, v0
	v_and_b32_e32 v2, 16, v0
	v_lshlrev_b32_e32 v0, 2, v0
	v_and_or_b32 v1, v1, 3, v175
	v_and_or_b32 v0, v0, 12, v2
	v_mul_u32_u24_e32 v1, 0x140, v1
	v_lshlrev_b32_e32 v0, 1, v0
	v_mov_b32_e32 v14, v163
	v_mov_b32_e32 v15, v163
	s_lshl_b32 s23, s69, 2
	s_ashr_i32 s68, s68, 7
	v_add3_u32 v178, 0, v1, v0
	v_mov_b32_e32 v0, v163
	v_mov_b32_e32 v1, v163
	v_mov_b32_e32 v2, v163
	v_mov_b32_e32 v3, v163
	v_mov_b32_e32 v4, v163
	v_mov_b32_e32 v5, v163
	v_mov_b32_e32 v6, v163
	v_mov_b32_e32 v7, v163
	v_mov_b32_e32 v8, v163
	v_mov_b32_e32 v9, v163
	v_mov_b32_e32 v10, v163
	v_mov_b32_e32 v11, v163
	v_mov_b32_e32 v12, v163
	v_mov_b32_e32 v13, v163
	v_mov_b64_e32 v[30:31], v[14:15]
	v_mov_b64_e32 v[46:47], v[14:15]
	v_mov_b64_e32 v[62:63], v[14:15]
	s_add_i32 s36, s23, 4
	s_or_b32 s37, s18, 0x80
	v_mad_u32_u24 v177, v170, s66, 0
	s_or_b32 s69, s18, 0xc0
	v_add_u32_e32 v179, 0xe800, v178
	v_or_b32_e32 v180, 2, v175
	v_or_b32_e32 v181, 3, v175
	v_or_b32_e32 v182, 8, v175
	v_or_b32_e32 v183, 9, v175
	v_or_b32_e32 v184, 10, v175
	v_or_b32_e32 v185, 11, v175
	v_or_b32_e32 v186, 16, v175
	v_or_b32_e32 v187, 17, v175
	v_or_b32_e32 v188, 18, v175
	v_or_b32_e32 v189, 19, v175
	v_or_b32_e32 v190, 24, v175
	v_or_b32_e32 v191, 25, v175
	v_or_b32_e32 v192, 26, v175
	v_or_b32_e32 v193, 27, v175
	v_add_u32_e32 v194, s24, v170
	s_add_i32 s70, s68, -1
	v_mov_b32_e32 v195, 0xf149f2ca
	v_mov_b32_e32 v64, 0
	s_mov_b32 s71, 0x7fffffc0
	v_mov_b64_e32 v[28:29], v[12:13]
	v_mov_b64_e32 v[26:27], v[10:11]
	v_mov_b64_e32 v[24:25], v[8:9]
	v_mov_b64_e32 v[22:23], v[6:7]
	v_mov_b64_e32 v[20:21], v[4:5]
	v_mov_b64_e32 v[18:19], v[2:3]
	v_mov_b64_e32 v[16:17], v[0:1]
	v_mov_b64_e32 v[44:45], v[12:13]
	v_mov_b64_e32 v[42:43], v[10:11]
	v_mov_b64_e32 v[40:41], v[8:9]
	v_mov_b64_e32 v[38:39], v[6:7]
	v_mov_b64_e32 v[36:37], v[4:5]
	v_mov_b64_e32 v[34:35], v[2:3]
	v_mov_b64_e32 v[32:33], v[0:1]
	v_mov_b64_e32 v[60:61], v[12:13]
	v_mov_b64_e32 v[58:59], v[10:11]
	v_mov_b64_e32 v[56:57], v[8:9]
	v_mov_b64_e32 v[54:55], v[6:7]
	v_mov_b64_e32 v[52:53], v[4:5]
	v_mov_b64_e32 v[50:51], v[2:3]
	v_mov_b64_e32 v[48:49], v[0:1]
	s_bitcmp1_b32 s92, 8
	s_cbranch_scc0 .Lmy_prio_0
	s_setprio 1
.Lmy_prio_0:
.LBB0_704:
	s_add_i32 s72, s33, 2
	s_cmp_ge_i32 s72, s36
	s_cselect_b64 s[28:29], -1, 0
	s_and_b64 vcc, exec, s[28:29]
	s_cbranch_vccnz .LBB0_706
	s_sub_i32 s0, s71, 64
	s_and_b32 s0, s0, 0x7fffff80
	s_cmp_eq_u32 s33, 0
	s_cselect_b32 s0, s37, s0
	s_add_u32 s0, s26, s0
	s_addc_u32 s1, s27, 0
	s_lshl_b64 s[0:1], s[0:1], 8
	s_add_u32 s2, s38, s0
	s_addc_u32 s3, s39, s1
	s_add_u32 s0, s40, s0
	s_addc_u32 s1, s41, s1
	v_lshl_add_u64 v[66:67], s[2:3], 0, v[164:165]
	v_lshl_add_u64 v[68:69], s[0:1], 0, v[164:165]
	global_load_dwordx4 v[150:153], v[66:67], off
	global_load_dwordx4 v[146:149], v[68:69], off
	v_lshl_add_u64 v[66:67], s[2:3], 0, v[166:167]
	v_lshl_add_u64 v[68:69], s[0:1], 0, v[166:167]
	global_load_dwordx4 v[158:161], v[66:67], off
	global_load_dwordx4 v[154:157], v[68:69], off

; __device__ __forceinline__ unsigned cvt_pk_bf16(float lo, float hi) { const bf16x2_t r = __builtin_convertvector((f32x2_t){lo, hi}, bf16x2_t); return __builtin_bit_cast(unsigned, r); }
; __device__ __forceinline__ void attn_unit(LAS unsigned char* lds, const bf16_t* Q, const bf16_t* K, const bf16_t* Vt, const float* kmean, bf16_t* mix,
;                                           const int b, const int h, const int blk, const int wv) {
;     ...
;     lsum += __shfl_xor(lsum, 32);
;     const float inv = 1.0f / lsum;
;     bf16_t* op = mix + qrow * DM + h * 128 + 4 * hh;
; #pragma unroll
;     for (int d = 0; d < 4; ++d)
; #pragma unroll
;         for (int rg = 0; rg < 4; ++rg) {
;             u32x2 wv; wv[0] = cvt_pk_bf16(o[d][4 * rg] * inv, o[d][4 * rg + 1] * inv); wv[1] = cvt_pk_bf16(o[d][4 * rg + 2] * inv, o[d][4 * rg + 3] * inv);
;             *(u32x2*)(op + 32 * d + 8 * rg) = wv;
;         }
.LBB0_766:
	s_setprio 0
	ds_bpermute_b32 v65, v171, v64
	s_ashr_i32 s0, s22, 3
	s_ashr_i32 s1, s0, 31
	s_lshl_b64 s[0:1], s[0:1], 11
	s_add_u32 s2, s0, s18
	s_waitcnt lgkmcnt(0)
	v_add_f32_e32 v66, v64, v65
	s_addc_u32 s3, s1, s67
	v_div_scale_f32 v67, s[0:1], v66, v66, 1.0
	v_rcp_f32_e32 v68, v67
	v_mov_b32_e32 v65, s3
	v_or_b32_e32 v64, s2, v170
	v_lshl_add_u64 v[64:65], v[64:65], 0, s[24:25]
	v_fma_f32 v69, -v67, v68, 1.0
	v_fmac_f32_e32 v68, v69, v68
	v_div_scale_f32 v69, vcc, 1.0, v66, 1.0
	v_mul_f32_e32 v70, v69, v68
	v_fma_f32 v71, -v67, v70, v69
	v_fmac_f32_e32 v70, v71, v68
	v_fma_f32 v67, -v67, v70, v69
	v_div_fmas_f32 v67, v67, v68, v70
	v_lshlrev_b64 v[64:65], 12, v[64:65]
	s_lshl_b32 s0, s22, 8
	v_div_fixup_f32 v66, v67, v66, 1.0
	v_lshl_add_u64 v[64:65], s[16:17], 0, v[64:65]
	s_and_b32 s18, s0, 0x700
	v_lshl_add_u64 v[64:65], v[64:65], 0, s[18:19]
	v_mov_b32_e32 v81, v163
	v_lshl_add_u64 v[64:65], v[80:81], 1, v[64:65]
	v_mbcnt_lo_u32_b32 v67, -1, 0
	v_mbcnt_hi_u32_b32 v67, -1, v67
	v_and_b32_e32 v67, 32, v67
	v_lshrrev_b32_e32 v68, 2, v67
	v_mov_b32_e32 v69, 0
	v_lshl_add_u64 v[64:65], v[64:65], 0, v[68:69]
	v_pk_mul_f32 v[48:49], v[48:49], v[66:67] op_sel_hi:[1,0]
	v_pk_mul_f32 v[50:51], v[50:51], v[66:67] op_sel_hi:[1,0]
	v_pk_mul_f32 v[52:53], v[52:53], v[66:67] op_sel_hi:[1,0]
	v_pk_mul_f32 v[54:55], v[54:55], v[66:67] op_sel_hi:[1,0]
	v_cvt_pk_bf16_f32 v48, v48, v49
	v_cvt_pk_bf16_f32 v49, v50, v51
	v_cvt_pk_bf16_f32 v50, v52, v53
	v_cvt_pk_bf16_f32 v51, v54, v55
	s_nop 1
	v_permlane32_swap_b32_e32 v48, v50
	v_permlane32_swap_b32_e32 v49, v51
	global_store_dwordx4 v[64:65], v[48:51], off
	v_pk_mul_f32 v[56:57], v[56:57], v[66:67] op_sel_hi:[1,0]
	v_pk_mul_f32 v[58:59], v[58:59], v[66:67] op_sel_hi:[1,0]
	v_pk_mul_f32 v[60:61], v[60:61], v[66:67] op_sel_hi:[1,0]
	v_pk_mul_f32 v[62:63], v[62:63], v[66:67] op_sel_hi:[1,0]
	v_cvt_pk_bf16_f32 v56, v56, v57
	v_cvt_pk_bf16_f32 v57, v58, v59
	v_cvt_pk_bf16_f32 v58, v60, v61
	v_cvt_pk_bf16_f32 v59, v62, v63
	s_nop 1
	v_permlane32_swap_b32_e32 v56, v58
	v_permlane32_swap_b32_e32 v57, v59
	global_store_dwordx4 v[64:65], v[56:59], off offset:32
	v_pk_mul_f32 v[32:33], v[32:33], v[66:67] op_sel_hi:[1,0]
	v_pk_mul_f32 v[34:35], v[34:35], v[66:67] op_sel_hi:[1,0]
	v_pk_mul_f32 v[36:37], v[36:37], v[66:67] op_sel_hi:[1,0]
	v_pk_mul_f32 v[38:39], v[38:39], v[66:67] op_sel_hi:[1,0]
	v_cvt_pk_bf16_f32 v32, v32, v33
	v_cvt_pk_bf16_f32 v33, v34, v35
	v_cvt_pk_bf16_f32 v34, v36, v37
	v_cvt_pk_bf16_f32 v35, v38, v39
	s_nop 1
	v_permlane32_swap_b32_e32 v32, v34
	v_permlane32_swap_b32_e32 v33, v35
	global_store_dwordx4 v[64:65], v[32:35], off offset:64
	v_pk_mul_f32 v[40:41], v[40:41], v[66:67] op_sel_hi:[1,0]
	v_pk_mul_f32 v[42:43], v[42:43], v[66:67] op_sel_hi:[1,0]
	v_pk_mul_f32 v[44:45], v[44:45], v[66:67] op_sel_hi:[1,0]
	v_pk_mul_f32 v[46:47], v[46:47], v[66:67] op_sel_hi:[1,0]
	v_cvt_pk_bf16_f32 v40, v40, v41
	v_cvt_pk_bf16_f32 v41, v42, v43
	v_cvt_pk_bf16_f32 v42, v44, v45
	v_cvt_pk_bf16_f32 v43, v46, v47
	s_nop 1
	v_permlane32_swap_b32_e32 v40, v42
	v_permlane32_swap_b32_e32 v41, v43
	global_store_dwordx4 v[64:65], v[40:43], off offset:96
	v_pk_mul_f32 v[16:17], v[16:17], v[66:67] op_sel_hi:[1,0]
	v_pk_mul_f32 v[18:19], v[18:19], v[66:67] op_sel_hi:[1,0]
	v_pk_mul_f32 v[20:21], v[20:21], v[66:67] op_sel_hi:[1,0]
	v_pk_mul_f32 v[22:23], v[22:23], v[66:67] op_sel_hi:[1,0]
	v_cvt_pk_bf16_f32 v16, v16, v17
	v_cvt_pk_bf16_f32 v17, v18, v19
	v_cvt_pk_bf16_f32 v18, v20, v21
	v_cvt_pk_bf16_f32 v19, v22, v23
	s_nop 1
	v_permlane32_swap_b32_e32 v16, v18
	v_permlane32_swap_b32_e32 v17, v19
	global_store_dwordx4 v[64:65], v[16:19], off offset:128
	v_pk_mul_f32 v[24:25], v[24:25], v[66:67] op_sel_hi:[1,0]
	v_pk_mul_f32 v[26:27], v[26:27], v[66:67] op_sel_hi:[1,0]
	v_pk_mul_f32 v[28:29], v[28:29], v[66:67] op_sel_hi:[1,0]
	v_pk_mul_f32 v[30:31], v[30:31], v[66:67] op_sel_hi:[1,0]
	v_cvt_pk_bf16_f32 v24, v24, v25
	v_cvt_pk_bf16_f32 v25, v26, v27
	v_cvt_pk_bf16_f32 v26, v28, v29
	v_cvt_pk_bf16_f32 v27, v30, v31
	s_nop 1
	v_permlane32_swap_b32_e32 v24, v26
	v_permlane32_swap_b32_e32 v25, v27
	global_store_dwordx4 v[64:65], v[24:27], off offset:160
	v_pk_mul_f32 v[0:1], v[0:1], v[66:67] op_sel_hi:[1,0]
	v_pk_mul_f32 v[2:3], v[2:3], v[66:67] op_sel_hi:[1,0]
	v_pk_mul_f32 v[4:5], v[4:5], v[66:67] op_sel_hi:[1,0]
	v_pk_mul_f32 v[6:7], v[6:7], v[66:67] op_sel_hi:[1,0]
	v_cvt_pk_bf16_f32 v0, v0, v1
	v_cvt_pk_bf16_f32 v1, v2, v3
	v_cvt_pk_bf16_f32 v2, v4, v5
	v_cvt_pk_bf16_f32 v3, v6, v7
	s_nop 1
	v_permlane32_swap_b32_e32 v0, v2
	v_permlane32_swap_b32_e32 v1, v3
	global_store_dwordx4 v[64:65], v[0:3], off offset:192
	v_pk_mul_f32 v[8:9], v[8:9], v[66:67] op_sel_hi:[1,0]
	v_pk_mul_f32 v[10:11], v[10:11], v[66:67] op_sel_hi:[1,0]
	v_pk_mul_f32 v[12:13], v[12:13], v[66:67] op_sel_hi:[1,0]
	v_pk_mul_f32 v[14:15], v[14:15], v[66:67] op_sel_hi:[1,0]
	v_cvt_pk_bf16_f32 v8, v8, v9
	v_cvt_pk_bf16_f32 v9, v10, v11
	v_cvt_pk_bf16_f32 v10, v12, v13
	v_cvt_pk_bf16_f32 v11, v14, v15
	s_nop 1
	v_permlane32_swap_b32_e32 v8, v10
	v_permlane32_swap_b32_e32 v9, v11
	global_store_dwordx4 v[64:65], v[8:11], off offset:224
	s_mov_b64 s[0:1], 0
	s_branch .LBB0_657

; __device__ __forceinline__ void attn_unit(LAS unsigned char* lds, const bf16_t* Q, const bf16_t* K, const bf16_t* Vt, const float* kmean, bf16_t* mix,
;                                           const int b, const int h, const int blk, const int wv) {
;     ...
;             g[n] = p + __shfl_xor(p, 32);
;         }
; #pragma unroll
;         for (int n = 0; n < 7; ++n) {
;             int rank = 0;
; #pragma unroll
;             for (int m2 = 0; m2 < 7; ++m2) if (m2 != n && m2 < blk) rank += (g[m2] > g[n] || (g[m2] == g[n] && m2 < n)) ? 1 : 0;
;             if (n < blk && rank < 3) sel |= 1u << n;
;         }
.LBB0_1774:
	s_andn2_b64 vcc, exec, s[36:37]
	s_mov_b32 s69, 0
	s_cbranch_vccnz .LBB0_1836
	v_add_f32_e32 v6, v70, v73
	v_add_f32_e32 v7, v71, v72
	v_add_f32_e32 v5, v75, v76
	v_cmp_gt_f32_e32 vcc, v6, v7
	v_add_f32_e32 v4, v74, v77
	s_and_b64 s[34:35], s[2:3], vcc
	v_cmp_gt_f32_e32 vcc, v5, v7
	v_add_f32_e32 v3, v79, v81
	v_cndmask_b32_e64 v8, 0, 1, s[34:35]
	s_and_b64 s[34:35], s[4:5], vcc
	v_cmp_gt_f32_e32 vcc, v4, v7
	v_add_f32_e32 v2, v78, v82
	v_cndmask_b32_e64 v9, 0, 1, s[34:35]
	s_and_b64 s[34:35], s[6:7], vcc
	v_cmp_gt_f32_e32 vcc, v3, v7
	v_add_f32_e32 v1, v83, v1
	v_add_u32_e32 v8, v9, v8
	v_cndmask_b32_e64 v9, 0, 1, s[34:35]
	s_and_b64 s[34:35], s[8:9], vcc
	v_cmp_gt_f32_e32 vcc, v2, v7
	v_cndmask_b32_e64 v10, 0, 1, s[34:35]
	s_and_b64 s[34:35], s[28:29], vcc
	v_cmp_gt_f32_e32 vcc, v1, v7
	v_add3_u32 v8, v8, v9, v10
	v_cndmask_b32_e64 v9, 0, 1, s[34:35]
	s_and_b64 s[34:35], s[30:31], vcc
	v_cndmask_b32_e64 v10, 0, 1, s[34:35]
	v_add3_u32 v8, v8, v9, v10
	v_cmp_gt_u32_e32 vcc, 3, v8
	s_and_b64 s[34:35], s[0:1], vcc
	v_cmp_ge_f32_e32 vcc, v7, v6
	v_cndmask_b32_e64 v8, 0, 1, s[34:35]
	s_and_b64 s[34:35], s[0:1], vcc
	v_cmp_gt_f32_e32 vcc, v5, v6
	v_cndmask_b32_e64 v9, 0, 1, s[34:35]
	s_and_b64 s[34:35], s[4:5], vcc
	v_cmp_gt_f32_e32 vcc, v4, v6
	v_cndmask_b32_e64 v10, 0, 1, s[34:35]
	s_and_b64 s[34:35], s[6:7], vcc
	v_cmp_gt_f32_e32 vcc, v3, v6
	v_add_u32_e32 v9, v10, v9
	v_cndmask_b32_e64 v10, 0, 1, s[34:35]
	s_and_b64 s[34:35], s[8:9], vcc
	v_cmp_gt_f32_e32 vcc, v2, v6
	v_cndmask_b32_e64 v11, 0, 1, s[34:35]
	s_and_b64 s[34:35], s[28:29], vcc
	v_cmp_gt_f32_e32 vcc, v1, v6
	v_add3_u32 v9, v9, v10, v11
	v_cndmask_b32_e64 v10, 0, 1, s[34:35]
	s_and_b64 s[34:35], s[30:31], vcc
	v_cndmask_b32_e64 v11, 0, 1, s[34:35]
	v_add3_u32 v9, v9, v10, v11
	v_cmp_gt_u32_e32 vcc, 3, v9
	s_and_b64 s[34:35], s[2:3], vcc
	v_cmp_ge_f32_e32 vcc, v7, v5
	v_cndmask_b32_e64 v9, 0, 2, s[34:35]
	s_and_b64 s[34:35], s[0:1], vcc
	v_cmp_ge_f32_e32 vcc, v6, v5
	v_cndmask_b32_e64 v10, 0, 1, s[34:35]
	s_and_b64 s[34:35], s[2:3], vcc
	v_cmp_gt_f32_e32 vcc, v4, v5
	v_cndmask_b32_e64 v11, 0, 1, s[34:35]
	s_and_b64 s[34:35], s[6:7], vcc
	v_cmp_gt_f32_e32 vcc, v3, v5
	v_add_u32_e32 v10, v10, v11
	v_cndmask_b32_e64 v11, 0, 1, s[34:35]
	s_and_b64 s[34:35], s[8:9], vcc
	v_cmp_gt_f32_e32 vcc, v2, v5
	v_cndmask_b32_e64 v12, 0, 1, s[34:35]
	s_and_b64 s[34:35], s[28:29], vcc
	v_cmp_gt_f32_e32 vcc, v1, v5
	v_add3_u32 v10, v10, v11, v12
	v_cndmask_b32_e64 v11, 0, 1, s[34:35]
	s_and_b64 s[34:35], s[30:31], vcc
	v_cndmask_b32_e64 v12, 0, 1, s[34:35]
	v_add3_u32 v10, v10, v11, v12
	v_cmp_gt_u32_e32 vcc, 3, v10
	s_and_b64 s[34:35], s[4:5], vcc
	v_cmp_ge_f32_e32 vcc, v7, v4
	v_cndmask_b32_e64 v10, 0, 4, s[34:35]
	s_and_b64 s[34:35], s[0:1], vcc
	v_cmp_ge_f32_e32 vcc, v6, v4
	v_or3_b32 v8, v9, v8, v10
	v_cndmask_b32_e64 v9, 0, 1, s[34:35]
	s_and_b64 s[34:35], s[2:3], vcc
	v_cmp_ge_f32_e32 vcc, v5, v4
	v_cndmask_b32_e64 v10, 0, 1, s[34:35]
	s_and_b64 s[34:35], s[4:5], vcc
	v_cmp_gt_f32_e32 vcc, v3, v4
	v_add_u32_e32 v9, v9, v10
	v_cndmask_b32_e64 v10, 0, 1, s[34:35]
	s_and_b64 s[34:35], s[8:9], vcc
	v_cmp_gt_f32_e32 vcc, v2, v4
	v_cndmask_b32_e64 v11, 0, 1, s[34:35]
	s_and_b64 s[34:35], s[28:29], vcc
	v_cmp_gt_f32_e32 vcc, v1, v4
	v_add3_u32 v9, v9, v10, v11
	v_cndmask_b32_e64 v10, 0, 1, s[34:35]
	s_and_b64 s[34:35], s[30:31], vcc
	v_cndmask_b32_e64 v11, 0, 1, s[34:35]
	v_add3_u32 v9, v9, v10, v11
	v_cmp_gt_u32_e32 vcc, 3, v9
	s_and_b64 s[34:35], s[6:7], vcc
	v_cmp_ge_f32_e32 vcc, v7, v3
	v_cndmask_b32_e64 v9, 0, 8, s[34:35]
	s_and_b64 s[34:35], s[0:1], vcc
	v_cmp_ge_f32_e32 vcc, v6, v3
	v_cndmask_b32_e64 v10, 0, 1, s[34:35]
	s_and_b64 s[34:35], s[2:3], vcc
	v_cmp_ge_f32_e32 vcc, v5, v3
	v_cndmask_b32_e64 v11, 0, 1, s[34:35]
	s_and_b64 s[34:35], s[4:5], vcc
	v_cmp_ge_f32_e32 vcc, v4, v3
	v_add_u32_e32 v10, v10, v11
	v_cndmask_b32_e64 v11, 0, 1, s[34:35]
	s_and_b64 s[34:35], s[6:7], vcc
	v_cmp_gt_f32_e32 vcc, v2, v3
	v_cndmask_b32_e64 v12, 0, 1, s[34:35]
	s_and_b64 s[34:35], s[28:29], vcc
	v_cmp_gt_f32_e32 vcc, v1, v3
	v_add3_u32 v10, v10, v11, v12
	v_cndmask_b32_e64 v11, 0, 1, s[34:35]
	s_and_b64 s[34:35], s[30:31], vcc
	v_cndmask_b32_e64 v12, 0, 1, s[34:35]
	v_add3_u32 v10, v10, v11, v12
	v_cmp_gt_u32_e32 vcc, 3, v10
	s_and_b64 s[34:35], s[8:9], vcc
	v_cmp_ge_f32_e32 vcc, v7, v2
	v_cndmask_b32_e64 v10, 0, 16, s[34:35]
	s_and_b64 s[34:35], s[0:1], vcc
	v_cmp_ge_f32_e32 vcc, v6, v2
	v_or3_b32 v8, v8, v9, v10
	v_cndmask_b32_e64 v9, 0, 1, s[34:35]
; #define ATT_LOAD(kr, vr, ti) do { const int _k0 = ATT_KEY0(ti); _Pragma("unroll") for (int _i = 0; _i < 2; ++_i) { const int _c = tid + 512 * _i; \
;         kr[_i] = *(const u32x4*)(K + (hbase + _k0) * 128 + (size_t)_c * 8); \
;         vr[_i] = *(const u32x4*)(Vt + (hbase + _k0) * 128 + (size_t)_c * 8); } } while (0)
; #define ATT_STORE(kr, vr, buf) do { _Pragma("unroll") for (int _i = 0; _i < 2; ++_i) { const int _c = tid + 512 * _i; \
;         *(LAS u32x4*)(lds + L_K + (buf) * KT_BYTES + (_c >> 4) * KSTR + (_c & 15) * 16) = kr[_i]; \
;         *(LAS u32x4*)(lds + L_V + (buf) * VT_BYTES + (_c >> 4) * VSTR + (_c & 15) * 16) = vr[_i]; } } while (0)
; __device__ __forceinline__ void attn_unit(LAS unsigned char* lds, const bf16_t* Q, const bf16_t* K, const bf16_t* Vt, const float* kmean, bf16_t* mix,
;                                           const int b, const int h, const int blk, const int wv) {
;     ...
;         for (int n = 0; n < 7; ++n) {
;             int rank = 0;
; #pragma unroll
;             for (int m2 = 0; m2 < 7; ++m2) if (m2 != n && m2 < blk) rank += (g[m2] > g[n] || (g[m2] == g[n] && m2 < n)) ? 1 : 0;
;             if (n < blk && rank < 3) sel |= 1u << n;
;         }
;     }
;     ATT_STORE(krA, vrA, 0);
;     if (ntile > 1) ATT_LOAD(krA, vrA, 1);
;     __syncthreads();
;     f32x16 o[4];
; #pragma unroll
;     for (int d = 0; d < 4; ++d)
; #pragma unroll
;         for (int r = 0; r < 16; ++r) o[d][r] = 0.f;
;     float mrun = -1e30f, lsum = 0.f;
	s_and_b64 s[34:35], s[2:3], vcc
	v_cmp_ge_f32_e32 vcc, v5, v2
	v_cndmask_b32_e64 v10, 0, 1, s[34:35]
	s_and_b64 s[34:35], s[4:5], vcc
	v_cmp_ge_f32_e32 vcc, v4, v2
	v_add_u32_e32 v9, v9, v10
	v_cndmask_b32_e64 v10, 0, 1, s[34:35]
	s_and_b64 s[34:35], s[6:7], vcc
	v_cmp_ge_f32_e32 vcc, v3, v2
	v_cndmask_b32_e64 v11, 0, 1, s[34:35]
	s_and_b64 s[34:35], s[8:9], vcc
	v_cmp_gt_f32_e32 vcc, v1, v2
	v_add3_u32 v9, v9, v10, v11
	v_cndmask_b32_e64 v10, 0, 1, s[34:35]
	s_and_b64 s[34:35], s[30:31], vcc
	v_cndmask_b32_e64 v11, 0, 1, s[34:35]
	v_add3_u32 v9, v9, v10, v11
	v_cmp_gt_u32_e32 vcc, 3, v9
	s_and_b64 s[34:35], s[28:29], vcc
	v_cmp_ge_f32_e32 vcc, v7, v1
	s_and_b64 s[0:1], s[0:1], vcc
	v_cmp_ge_f32_e32 vcc, v6, v1
	v_cndmask_b32_e64 v7, 0, 1, s[0:1]
	s_and_b64 s[0:1], s[2:3], vcc
	v_cmp_ge_f32_e32 vcc, v5, v1
	v_cndmask_b32_e64 v6, 0, 1, s[0:1]
	s_and_b64 s[0:1], s[4:5], vcc
	v_cmp_ge_f32_e32 vcc, v4, v1
	v_cndmask_b32_e64 v5, 0, 1, s[0:1]
	s_and_b64 s[0:1], s[6:7], vcc
	v_cmp_ge_f32_e32 vcc, v3, v1
	v_cndmask_b32_e64 v4, 0, 1, s[0:1]
	s_and_b64 s[0:1], s[8:9], vcc
	v_cmp_ge_f32_e32 vcc, v2, v1
	v_add_u32_e32 v6, v7, v6
	v_cndmask_b32_e64 v3, 0, 1, s[0:1]
	s_and_b64 s[0:1], s[28:29], vcc
	v_add3_u32 v4, v6, v5, v4
	v_cndmask_b32_e64 v1, 0, 1, s[0:1]
	v_add3_u32 v1, v4, v3, v1
	v_cmp_gt_u32_e32 vcc, 3, v1
	s_and_b64 s[0:1], s[30:31], vcc
	v_cndmask_b32_e64 v9, 0, 32, s[34:35]
	v_cndmask_b32_e64 v1, 0, 64, s[0:1]
	v_or3_b32 v176, v8, v9, v1
	v_lshrrev_b32_e32 v1, 2, v0
	v_and_b32_e32 v2, 16, v0
	v_lshlrev_b32_e32 v0, 2, v0
	v_and_or_b32 v1, v1, 3, v175
	v_and_or_b32 v0, v0, 12, v2
	v_mul_u32_u24_e32 v1, 0x140, v1
	v_lshlrev_b32_e32 v0, 1, v0
	v_mov_b32_e32 v14, v163
	v_mov_b32_e32 v15, v163
	s_lshl_b32 s23, s33, 2
	s_ashr_i32 s37, s65, 7
	v_add3_u32 v178, 0, v1, v0
	v_mov_b32_e32 v0, v163
	v_mov_b32_e32 v1, v163
	v_mov_b32_e32 v2, v163
	v_mov_b32_e32 v3, v163
	v_mov_b32_e32 v4, v163
	v_mov_b32_e32 v5, v163
	v_mov_b32_e32 v6, v163
	v_mov_b32_e32 v7, v163
	v_mov_b32_e32 v8, v163
	v_mov_b32_e32 v9, v163
	v_mov_b32_e32 v10, v163
	v_mov_b32_e32 v11, v163
	v_mov_b32_e32 v12, v163
	v_mov_b32_e32 v13, v163
	v_mov_b64_e32 v[30:31], v[14:15]
	v_mov_b64_e32 v[46:47], v[14:15]
	v_mov_b64_e32 v[62:63], v[14:15]
	s_add_i32 s33, s23, 4
	s_or_b32 s36, s18, 0x80
	v_mad_u32_u24 v177, v170, s63, 0
	s_or_b32 s65, s18, 0xc0
	v_add_u32_e32 v179, 0xe800, v178
	v_or_b32_e32 v180, 2, v175
	v_or_b32_e32 v181, 3, v175
	v_or_b32_e32 v182, 8, v175
	v_or_b32_e32 v183, 9, v175
	v_or_b32_e32 v184, 10, v175
	v_or_b32_e32 v185, 11, v175
	v_or_b32_e32 v186, 16, v175
	v_or_b32_e32 v187, 17, v175
	v_or_b32_e32 v188, 18, v175
	v_or_b32_e32 v189, 19, v175
	v_or_b32_e32 v190, 24, v175
	v_or_b32_e32 v191, 25, v175
	v_or_b32_e32 v192, 26, v175
	v_or_b32_e32 v193, 27, v175
	v_add_u32_e32 v194, s24, v170
	s_add_i32 s66, s37, -1
	v_mov_b32_e32 v195, 0xf149f2ca
	v_mov_b32_e32 v64, 0
	s_mov_b32 s67, 0x7fffffc0
	v_mov_b64_e32 v[28:29], v[12:13]
	v_mov_b64_e32 v[26:27], v[10:11]
	v_mov_b64_e32 v[24:25], v[8:9]
	v_mov_b64_e32 v[22:23], v[6:7]
	v_mov_b64_e32 v[20:21], v[4:5]
	v_mov_b64_e32 v[18:19], v[2:3]
	v_mov_b64_e32 v[16:17], v[0:1]
	v_mov_b64_e32 v[44:45], v[12:13]
	v_mov_b64_e32 v[42:43], v[10:11]
	v_mov_b64_e32 v[40:41], v[8:9]
	v_mov_b64_e32 v[38:39], v[6:7]
	v_mov_b64_e32 v[36:37], v[4:5]
	v_mov_b64_e32 v[34:35], v[2:3]
	v_mov_b64_e32 v[32:33], v[0:1]
	v_mov_b64_e32 v[60:61], v[12:13]
	v_mov_b64_e32 v[58:59], v[10:11]
	v_mov_b64_e32 v[56:57], v[8:9]
	v_mov_b64_e32 v[54:55], v[6:7]
	v_mov_b64_e32 v[52:53], v[4:5]
	v_mov_b64_e32 v[50:51], v[2:3]
	v_mov_b64_e32 v[48:49], v[0:1]
	s_bitcmp1_b32 s92, 8
	s_cbranch_scc0 .Lmy_prio_1
	s_setprio 1
.Lmy_prio_1:
.LBB0_1776:
	s_add_i32 s68, s69, 2
	s_cmp_ge_i32 s68, s33
	s_cselect_b64 s[2:3], -1, 0
	s_and_b64 vcc, exec, s[2:3]
	s_cbranch_vccnz .LBB0_1778
	s_sub_i32 s0, s67, 64
	s_and_b32 s0, s0, 0x7fffff80
	s_cmp_eq_u32 s69, 0
	s_cselect_b32 s0, s36, s0
	s_add_u32 s0, s26, s0
	s_addc_u32 s1, s27, 0
	s_lshl_b64 s[0:1], s[0:1], 8
	s_add_u32 s4, s38, s0
	s_addc_u32 s5, s39, s1
	s_add_u32 s0, s40, s0
	s_addc_u32 s1, s41, s1
	v_lshl_add_u64 v[66:67], s[4:5], 0, v[164:165]
	v_lshl_add_u64 v[68:69], s[0:1], 0, v[164:165]
	global_load_dwordx4 v[150:153], v[66:67], off
	global_load_dwordx4 v[146:149], v[68:69], off
	v_lshl_add_u64 v[66:67], s[4:5], 0, v[166:167]
	v_lshl_add_u64 v[68:69], s[0:1], 0, v[166:167]
	global_load_dwordx4 v[158:161], v[66:67], off
	global_load_dwordx4 v[154:157], v[68:69], off

; __device__ __forceinline__ unsigned cvt_pk_bf16(float lo, float hi) { const bf16x2_t r = __builtin_convertvector((f32x2_t){lo, hi}, bf16x2_t); return __builtin_bit_cast(unsigned, r); }
; __device__ __forceinline__ void attn_unit(LAS unsigned char* lds, const bf16_t* Q, const bf16_t* K, const bf16_t* Vt, const float* kmean, bf16_t* mix,
;                                           const int b, const int h, const int blk, const int wv) {
;     ...
;     lsum += __shfl_xor(lsum, 32);
;     const float inv = 1.0f / lsum;
;     bf16_t* op = mix + qrow * DM + h * 128 + 4 * hh;
; #pragma unroll
;     for (int d = 0; d < 4; ++d)
; #pragma unroll
;         for (int rg = 0; rg < 4; ++rg) {
;             u32x2 wv; wv[0] = cvt_pk_bf16(o[d][4 * rg] * inv, o[d][4 * rg + 1] * inv); wv[1] = cvt_pk_bf16(o[d][4 * rg + 2] * inv, o[d][4 * rg + 3] * inv);
;             *(u32x2*)(op + 32 * d + 8 * rg) = wv;
;         }
.LBB0_1838:
	s_setprio 0
	ds_bpermute_b32 v65, v171, v64
	s_ashr_i32 s0, s22, 3
	s_ashr_i32 s1, s0, 31
	s_lshl_b64 s[0:1], s[0:1], 11
	s_add_u32 s2, s0, s18
	s_waitcnt lgkmcnt(0)
	v_add_f32_e32 v66, v64, v65
	s_addc_u32 s3, s1, s64
	v_div_scale_f32 v67, s[0:1], v66, v66, 1.0
	v_rcp_f32_e32 v68, v67
	v_mov_b32_e32 v65, s3
	v_or_b32_e32 v64, s2, v170
	v_lshl_add_u64 v[64:65], v[64:65], 0, s[24:25]
	v_fma_f32 v69, -v67, v68, 1.0
	v_fmac_f32_e32 v68, v69, v68
	v_div_scale_f32 v69, vcc, 1.0, v66, 1.0
	v_mul_f32_e32 v70, v69, v68
	v_fma_f32 v71, -v67, v70, v69
	v_fmac_f32_e32 v70, v71, v68
	v_fma_f32 v67, -v67, v70, v69
	v_div_fmas_f32 v67, v67, v68, v70
	v_lshlrev_b64 v[64:65], 12, v[64:65]
	s_lshl_b32 s0, s22, 8
	v_div_fixup_f32 v66, v67, v66, 1.0
	v_lshl_add_u64 v[64:65], s[16:17], 0, v[64:65]
	s_and_b32 s18, s0, 0x700
	v_lshl_add_u64 v[64:65], v[64:65], 0, s[18:19]
	v_mov_b32_e32 v81, v163
	v_lshl_add_u64 v[64:65], v[80:81], 1, v[64:65]
	v_mbcnt_lo_u32_b32 v67, -1, 0
	v_mbcnt_hi_u32_b32 v67, -1, v67
	v_and_b32_e32 v67, 32, v67
	v_lshrrev_b32_e32 v68, 2, v67
	v_mov_b32_e32 v69, 0
	v_lshl_add_u64 v[64:65], v[64:65], 0, v[68:69]
	v_pk_mul_f32 v[48:49], v[48:49], v[66:67] op_sel_hi:[1,0]
	v_pk_mul_f32 v[50:51], v[50:51], v[66:67] op_sel_hi:[1,0]
	v_pk_mul_f32 v[52:53], v[52:53], v[66:67] op_sel_hi:[1,0]
	v_pk_mul_f32 v[54:55], v[54:55], v[66:67] op_sel_hi:[1,0]
	v_cvt_pk_bf16_f32 v48, v48, v49
	v_cvt_pk_bf16_f32 v49, v50, v51
	v_cvt_pk_bf16_f32 v50, v52, v53
	v_cvt_pk_bf16_f32 v51, v54, v55
	s_nop 1
	v_permlane32_swap_b32_e32 v48, v50
	v_permlane32_swap_b32_e32 v49, v51
	global_store_dwordx4 v[64:65], v[48:51], off
	v_pk_mul_f32 v[56:57], v[56:57], v[66:67] op_sel_hi:[1,0]
	v_pk_mul_f32 v[58:59], v[58:59], v[66:67] op_sel_hi:[1,0]
	v_pk_mul_f32 v[60:61], v[60:61], v[66:67] op_sel_hi:[1,0]
	v_pk_mul_f32 v[62:63], v[62:63], v[66:67] op_sel_hi:[1,0]
	v_cvt_pk_bf16_f32 v56, v56, v57
	v_cvt_pk_bf16_f32 v57, v58, v59
	v_cvt_pk_bf16_f32 v58, v60, v61
	v_cvt_pk_bf16_f32 v59, v62, v63
	s_nop 1
	v_permlane32_swap_b32_e32 v56, v58
	v_permlane32_swap_b32_e32 v57, v59
	global_store_dwordx4 v[64:65], v[56:59], off offset:32
	v_pk_mul_f32 v[32:33], v[32:33], v[66:67] op_sel_hi:[1,0]
	v_pk_mul_f32 v[34:35], v[34:35], v[66:67] op_sel_hi:[1,0]
	v_pk_mul_f32 v[36:37], v[36:37], v[66:67] op_sel_hi:[1,0]
	v_pk_mul_f32 v[38:39], v[38:39], v[66:67] op_sel_hi:[1,0]
	v_cvt_pk_bf16_f32 v32, v32, v33
	v_cvt_pk_bf16_f32 v33, v34, v35
	v_cvt_pk_bf16_f32 v34, v36, v37
	v_cvt_pk_bf16_f32 v35, v38, v39
	s_nop 1
	v_permlane32_swap_b32_e32 v32, v34
	v_permlane32_swap_b32_e32 v33, v35
	global_store_dwordx4 v[64:65], v[32:35], off offset:64
	v_pk_mul_f32 v[40:41], v[40:41], v[66:67] op_sel_hi:[1,0]
	v_pk_mul_f32 v[42:43], v[42:43], v[66:67] op_sel_hi:[1,0]
	v_pk_mul_f32 v[44:45], v[44:45], v[66:67] op_sel_hi:[1,0]
	v_pk_mul_f32 v[46:47], v[46:47], v[66:67] op_sel_hi:[1,0]
	v_cvt_pk_bf16_f32 v40, v40, v41
	v_cvt_pk_bf16_f32 v41, v42, v43
	v_cvt_pk_bf16_f32 v42, v44, v45
	v_cvt_pk_bf16_f32 v43, v46, v47
	s_nop 1
	v_permlane32_swap_b32_e32 v40, v42
	v_permlane32_swap_b32_e32 v41, v43
	global_store_dwordx4 v[64:65], v[40:43], off offset:96
	v_pk_mul_f32 v[16:17], v[16:17], v[66:67] op_sel_hi:[1,0]
	v_pk_mul_f32 v[18:19], v[18:19], v[66:67] op_sel_hi:[1,0]
	v_pk_mul_f32 v[20:21], v[20:21], v[66:67] op_sel_hi:[1,0]
	v_pk_mul_f32 v[22:23], v[22:23], v[66:67] op_sel_hi:[1,0]
	v_cvt_pk_bf16_f32 v16, v16, v17
	v_cvt_pk_bf16_f32 v17, v18, v19
	v_cvt_pk_bf16_f32 v18, v20, v21
	v_cvt_pk_bf16_f32 v19, v22, v23
	s_nop 1
	v_permlane32_swap_b32_e32 v16, v18
	v_permlane32_swap_b32_e32 v17, v19
	global_store_dwordx4 v[64:65], v[16:19], off offset:128
	v_pk_mul_f32 v[24:25], v[24:25], v[66:67] op_sel_hi:[1,0]
	v_pk_mul_f32 v[26:27], v[26:27], v[66:67] op_sel_hi:[1,0]
	v_pk_mul_f32 v[28:29], v[28:29], v[66:67] op_sel_hi:[1,0]
	v_pk_mul_f32 v[30:31], v[30:31], v[66:67] op_sel_hi:[1,0]
	v_cvt_pk_bf16_f32 v24, v24, v25
	v_cvt_pk_bf16_f32 v25, v26, v27
	v_cvt_pk_bf16_f32 v26, v28, v29
	v_cvt_pk_bf16_f32 v27, v30, v31
	s_nop 1
	v_permlane32_swap_b32_e32 v24, v26
	v_permlane32_swap_b32_e32 v25, v27
	global_store_dwordx4 v[64:65], v[24:27], off offset:160
	v_pk_mul_f32 v[0:1], v[0:1], v[66:67] op_sel_hi:[1,0]
	v_pk_mul_f32 v[2:3], v[2:3], v[66:67] op_sel_hi:[1,0]
	v_pk_mul_f32 v[4:5], v[4:5], v[66:67] op_sel_hi:[1,0]
	v_pk_mul_f32 v[6:7], v[6:7], v[66:67] op_sel_hi:[1,0]
	v_cvt_pk_bf16_f32 v0, v0, v1
	v_cvt_pk_bf16_f32 v1, v2, v3
	v_cvt_pk_bf16_f32 v2, v4, v5
	v_cvt_pk_bf16_f32 v3, v6, v7
	s_nop 1
	v_permlane32_swap_b32_e32 v0, v2
	v_permlane32_swap_b32_e32 v1, v3
	global_store_dwordx4 v[64:65], v[0:3], off offset:192
	v_pk_mul_f32 v[8:9], v[8:9], v[66:67] op_sel_hi:[1,0]
	v_pk_mul_f32 v[10:11], v[10:11], v[66:67] op_sel_hi:[1,0]
	v_pk_mul_f32 v[12:13], v[12:13], v[66:67] op_sel_hi:[1,0]
	v_pk_mul_f32 v[14:15], v[14:15], v[66:67] op_sel_hi:[1,0]
	v_cvt_pk_bf16_f32 v8, v8, v9
	v_cvt_pk_bf16_f32 v9, v10, v11
	v_cvt_pk_bf16_f32 v10, v12, v13
	v_cvt_pk_bf16_f32 v11, v14, v15
	s_nop 1
	v_permlane32_swap_b32_e32 v8, v10
	v_permlane32_swap_b32_e32 v9, v11
	global_store_dwordx4 v[64:65], v[8:11], off offset:224
	s_mov_b64 s[0:1], 0
	s_branch .LBB0_1714
